# baseline (speedup 1.0000x reference)
.LBB2_6:
	s_load_dwordx2 s[20:21], s[0:1], 0x0
	s_load_dwordx4 s[24:27], s[0:1], 0x10
	s_mov_b32 s16, s10
	s_mov_b32 s17, s9
	v_mov_b32_e32 v165, v130
	s_lshl_b32 s18, s16, 18
	s_lshl_b32 s19, s17, 17
	s_add_u32 s18, s18, s19
	v_lshl_or_b32 v164, s17, 13, v165
	v_lshlrev_b32_e32 v2, 2, v0
	s_lshl_b32 s28, s16, 9
	s_waitcnt lgkmcnt(0)
	s_add_u32 s20, s20, s18
	s_addc_u32 s21, s21, 0
	s_add_u32 s22, s20, 0x10000
	s_addc_u32 s23, s21, 0
	s_add_u32 s24, s24, s28
	s_addc_u32 s25, s25, 0
	s_add_u32 s26, s26, s28
	s_addc_u32 s27, s27, 0
	global_load_dword v1, v2, s[24:25] offset:-1024
	global_load_dword v3, v2, s[26:27] offset:-1024
	global_load_dwordx4 v[4:7], v165, s[20:21]
	global_load_dwordx4 v[8:11], v165, s[20:21] offset:1024
	global_load_dwordx4 v[12:15], v165, s[20:21] offset:2048
	global_load_dwordx4 v[16:19], v165, s[20:21] offset:3072
	global_load_dwordx4 v[20:23], v165, s[22:23]
	global_load_dwordx4 v[24:27], v165, s[22:23] offset:1024
	global_load_dwordx4 v[28:31], v165, s[22:23] offset:2048
	global_load_dwordx4 v[32:35], v165, s[22:23] offset:3072
	s_add_u32 s20, s20, 0x1000
	s_addc_u32 s21, s21, 0
	s_add_u32 s22, s22, 0x1000
	s_addc_u32 s23, s23, 0
	global_load_dwordx4 v[36:39], v165, s[20:21]
	global_load_dwordx4 v[40:43], v165, s[20:21] offset:1024
	global_load_dwordx4 v[44:47], v165, s[20:21] offset:2048
	global_load_dwordx4 v[48:51], v165, s[20:21] offset:3072
	global_load_dwordx4 v[52:55], v165, s[22:23]
	global_load_dwordx4 v[56:59], v165, s[22:23] offset:1024
	global_load_dwordx4 v[60:63], v165, s[22:23] offset:2048
	global_load_dwordx4 v[64:67], v165, s[22:23] offset:3072
	s_add_u32 s20, s20, 0x1000
	s_addc_u32 s21, s21, 0
	s_add_u32 s22, s22, 0x1000
	s_addc_u32 s23, s23, 0
	global_load_dwordx4 v[68:71], v165, s[20:21]
	global_load_dwordx4 v[72:75], v165, s[20:21] offset:1024
	global_load_dwordx4 v[76:79], v165, s[20:21] offset:2048
	global_load_dwordx4 v[80:83], v165, s[20:21] offset:3072
	global_load_dwordx4 v[84:87], v165, s[22:23]
	global_load_dwordx4 v[88:91], v165, s[22:23] offset:1024
	global_load_dwordx4 v[92:95], v165, s[22:23] offset:2048
	global_load_dwordx4 v[96:99], v165, s[22:23] offset:3072
	s_add_u32 s20, s20, 0x1000
	s_addc_u32 s21, s21, 0
	s_add_u32 s22, s22, 0x1000
	s_addc_u32 s23, s23, 0
	global_load_dwordx4 v[100:103], v165, s[20:21]
	global_load_dwordx4 v[104:107], v165, s[20:21] offset:1024
	global_load_dwordx4 v[108:111], v165, s[20:21] offset:2048
	global_load_dwordx4 v[112:115], v165, s[20:21] offset:3072
	global_load_dwordx4 v[116:119], v165, s[22:23]
	global_load_dwordx4 v[120:123], v165, s[22:23] offset:1024
	global_load_dwordx4 v[124:127], v165, s[22:23] offset:2048
	global_load_dwordx4 v[128:131], v165, s[22:23] offset:3072
	s_add_u32 s20, s20, 0x1000
	s_addc_u32 s21, s21, 0
	s_add_u32 s22, s22, 0x1000
	s_addc_u32 s23, s23, 0
	global_load_dwordx4 v[132:135], v165, s[20:21]
	global_load_dwordx4 v[136:139], v165, s[20:21] offset:1024
	global_load_dwordx4 v[140:143], v165, s[20:21] offset:2048
	global_load_dwordx4 v[144:147], v165, s[20:21] offset:3072
	global_load_dwordx4 v[148:151], v165, s[22:23]
	global_load_dwordx4 v[152:155], v165, s[22:23] offset:1024
	global_load_dwordx4 v[156:159], v165, s[22:23] offset:2048
	global_load_dwordx4 v[160:163], v165, s[22:23] offset:3072
	s_add_u32 s20, s20, 0x1000
	s_addc_u32 s21, s21, 0
	s_add_u32 s22, s22, 0x1000
	s_addc_u32 s23, s23, 0
	s_waitcnt vmcnt(40)
	v_mul_f32_e32 v1, 0x4038aa3b, v1
	ds_write2st64_b32 v2, v1, v3 offset0:124 offset1:126
	s_waitcnt vmcnt(39)
	ds_write_b128 v164, v[4:7]
	s_waitcnt vmcnt(38)
	ds_write_b128 v164, v[8:11] offset:1024
	s_waitcnt vmcnt(37)
	ds_write_b128 v164, v[12:15] offset:2048
	s_waitcnt vmcnt(36)
	ds_write_b128 v164, v[16:19] offset:3072
	s_waitcnt vmcnt(35)
	ds_write_b128 v164, v[20:23] offset:4096
	s_waitcnt vmcnt(34)
	ds_write_b128 v164, v[24:27] offset:5120
	s_waitcnt vmcnt(33)
	ds_write_b128 v164, v[28:31] offset:6144
	s_waitcnt vmcnt(32)
	ds_write_b128 v164, v[32:35] offset:7168
	s_waitcnt lgkmcnt(0)
	s_barrier
	global_load_dwordx4 v[4:7], v165, s[20:21]
	global_load_dwordx4 v[8:11], v165, s[20:21] offset:1024
	global_load_dwordx4 v[12:15], v165, s[20:21] offset:2048
	global_load_dwordx4 v[16:19], v165, s[20:21] offset:3072
	global_load_dwordx4 v[20:23], v165, s[22:23]
	global_load_dwordx4 v[24:27], v165, s[22:23] offset:1024
	global_load_dwordx4 v[28:31], v165, s[22:23] offset:2048
	global_load_dwordx4 v[32:35], v165, s[22:23] offset:3072
	s_add_u32 s20, s20, 0x1000
	s_addc_u32 s21, s21, 0
	s_add_u32 s22, s22, 0x1000
	s_addc_u32 s23, s23, 0
	s_waitcnt vmcnt(39)
	ds_write_b128 v164, v[36:39] offset:16384
	s_waitcnt vmcnt(38)
	ds_write_b128 v164, v[40:43] offset:17408
	s_waitcnt vmcnt(37)
	ds_write_b128 v164, v[44:47] offset:18432
	s_waitcnt vmcnt(36)
	ds_write_b128 v164, v[48:51] offset:19456
	s_waitcnt vmcnt(35)
	ds_write_b128 v164, v[52:55] offset:20480
	s_waitcnt vmcnt(34)
	ds_write_b128 v164, v[56:59] offset:21504
	s_waitcnt vmcnt(33)
	ds_write_b128 v164, v[60:63] offset:22528
	s_waitcnt vmcnt(32)
	ds_write_b128 v164, v[64:67] offset:23552
	s_waitcnt lgkmcnt(0)
	s_barrier
	global_load_dwordx4 v[36:39], v165, s[20:21]
	global_load_dwordx4 v[40:43], v165, s[20:21] offset:1024
	global_load_dwordx4 v[44:47], v165, s[20:21] offset:2048
	global_load_dwordx4 v[48:51], v165, s[20:21] offset:3072
	global_load_dwordx4 v[52:55], v165, s[22:23]
	global_load_dwordx4 v[56:59], v165, s[22:23] offset:1024
	global_load_dwordx4 v[60:63], v165, s[22:23] offset:2048
	global_load_dwordx4 v[64:67], v165, s[22:23] offset:3072
	s_add_u32 s20, s20, 0x1000
	s_addc_u32 s21, s21, 0
	s_add_u32 s22, s22, 0x1000
	s_addc_u32 s23, s23, 0
	s_waitcnt vmcnt(39)
	ds_write_b128 v164, v[68:71]
	s_waitcnt vmcnt(38)
	ds_write_b128 v164, v[72:75] offset:1024
	s_waitcnt vmcnt(37)
	ds_write_b128 v164, v[76:79] offset:2048
	s_waitcnt vmcnt(36)
	ds_write_b128 v164, v[80:83] offset:3072
	s_waitcnt vmcnt(35)
	ds_write_b128 v164, v[84:87] offset:4096
	s_waitcnt vmcnt(34)
	ds_write_b128 v164, v[88:91] offset:5120
	s_waitcnt vmcnt(33)
	ds_write_b128 v164, v[92:95] offset:6144
	s_waitcnt vmcnt(32)
	ds_write_b128 v164, v[96:99] offset:7168
	s_waitcnt lgkmcnt(0)
	s_barrier
	global_load_dwordx4 v[68:71], v165, s[20:21]
	global_load_dwordx4 v[72:75], v165, s[20:21] offset:1024
	global_load_dwordx4 v[76:79], v165, s[20:21] offset:2048
	global_load_dwordx4 v[80:83], v165, s[20:21] offset:3072
	global_load_dwordx4 v[84:87], v165, s[22:23]
	global_load_dwordx4 v[88:91], v165, s[22:23] offset:1024
	global_load_dwordx4 v[92:95], v165, s[22:23] offset:2048
	global_load_dwordx4 v[96:99], v165, s[22:23] offset:3072
	s_add_u32 s20, s20, 0x1000
	s_addc_u32 s21, s21, 0
	s_add_u32 s22, s22, 0x1000
	s_addc_u32 s23, s23, 0
	s_waitcnt vmcnt(39)
	ds_write_b128 v164, v[100:103] offset:16384
	s_waitcnt vmcnt(38)
	ds_write_b128 v164, v[104:107] offset:17408
	s_waitcnt vmcnt(37)
	ds_write_b128 v164, v[108:111] offset:18432
	s_waitcnt vmcnt(36)
	ds_write_b128 v164, v[112:115] offset:19456
	s_waitcnt vmcnt(35)
	ds_write_b128 v164, v[116:119] offset:20480
	s_waitcnt vmcnt(34)
	ds_write_b128 v164, v[120:123] offset:21504
	s_waitcnt vmcnt(33)
	ds_write_b128 v164, v[124:127] offset:22528
	s_waitcnt vmcnt(32)
	ds_write_b128 v164, v[128:131] offset:23552
	s_waitcnt lgkmcnt(0)
	s_barrier
	global_load_dwordx4 v[100:103], v165, s[20:21]
	global_load_dwordx4 v[104:107], v165, s[20:21] offset:1024
	global_load_dwordx4 v[108:111], v165, s[20:21] offset:2048
	global_load_dwordx4 v[112:115], v165, s[20:21] offset:3072
	global_load_dwordx4 v[116:119], v165, s[22:23]
	global_load_dwordx4 v[120:123], v165, s[22:23] offset:1024
	global_load_dwordx4 v[124:127], v165, s[22:23] offset:2048
	global_load_dwordx4 v[128:131], v165, s[22:23] offset:3072
	s_add_u32 s20, s20, 0x1000
	s_addc_u32 s21, s21, 0
	s_add_u32 s22, s22, 0x1000
	s_addc_u32 s23, s23, 0
	s_waitcnt vmcnt(39)
	ds_write_b128 v164, v[132:135]
	s_waitcnt vmcnt(38)
	ds_write_b128 v164, v[136:139] offset:1024
	s_waitcnt vmcnt(37)
	ds_write_b128 v164, v[140:143] offset:2048
	s_waitcnt vmcnt(36)
	ds_write_b128 v164, v[144:147] offset:3072
	s_waitcnt vmcnt(35)
	ds_write_b128 v164, v[148:151] offset:4096
	s_waitcnt vmcnt(34)
	ds_write_b128 v164, v[152:155] offset:5120
	s_waitcnt vmcnt(33)
	ds_write_b128 v164, v[156:159] offset:6144
	s_waitcnt vmcnt(32)
	ds_write_b128 v164, v[160:163] offset:7168
	s_waitcnt lgkmcnt(0)
	s_barrier
	global_load_dwordx4 v[132:135], v165, s[20:21]
	global_load_dwordx4 v[136:139], v165, s[20:21] offset:1024
	global_load_dwordx4 v[140:143], v165, s[20:21] offset:2048
	global_load_dwordx4 v[144:147], v165, s[20:21] offset:3072
	global_load_dwordx4 v[148:151], v165, s[22:23]
	global_load_dwordx4 v[152:155], v165, s[22:23] offset:1024
	global_load_dwordx4 v[156:159], v165, s[22:23] offset:2048
	global_load_dwordx4 v[160:163], v165, s[22:23] offset:3072
	s_add_u32 s20, s20, 0x1000
	s_addc_u32 s21, s21, 0
	s_add_u32 s22, s22, 0x1000
	s_addc_u32 s23, s23, 0
	s_waitcnt vmcnt(39)
	ds_write_b128 v164, v[4:7] offset:16384
	s_waitcnt vmcnt(38)
	ds_write_b128 v164, v[8:11] offset:17408
	s_waitcnt vmcnt(37)
	ds_write_b128 v164, v[12:15] offset:18432
	s_waitcnt vmcnt(36)
	ds_write_b128 v164, v[16:19] offset:19456
	s_waitcnt vmcnt(35)
	ds_write_b128 v164, v[20:23] offset:20480
	s_waitcnt vmcnt(34)
	ds_write_b128 v164, v[24:27] offset:21504
	s_waitcnt vmcnt(33)
	ds_write_b128 v164, v[28:31] offset:22528
	s_waitcnt vmcnt(32)
	ds_write_b128 v164, v[32:35] offset:23552
	s_waitcnt lgkmcnt(0)
	s_barrier
	global_load_dwordx4 v[4:7], v165, s[20:21]
	global_load_dwordx4 v[8:11], v165, s[20:21] offset:1024
	global_load_dwordx4 v[12:15], v165, s[20:21] offset:2048
	global_load_dwordx4 v[16:19], v165, s[20:21] offset:3072
	global_load_dwordx4 v[20:23], v165, s[22:23]
	global_load_dwordx4 v[24:27], v165, s[22:23] offset:1024
	global_load_dwordx4 v[28:31], v165, s[22:23] offset:2048
	global_load_dwordx4 v[32:35], v165, s[22:23] offset:3072
	s_add_u32 s20, s20, 0x1000
	s_addc_u32 s21, s21, 0
	s_add_u32 s22, s22, 0x1000
	s_addc_u32 s23, s23, 0
	s_waitcnt vmcnt(39)
	ds_write_b128 v164, v[36:39]
	s_waitcnt vmcnt(38)
	ds_write_b128 v164, v[40:43] offset:1024
	s_waitcnt vmcnt(37)
	ds_write_b128 v164, v[44:47] offset:2048
	s_waitcnt vmcnt(36)
	ds_write_b128 v164, v[48:51] offset:3072
	s_waitcnt vmcnt(35)
	ds_write_b128 v164, v[52:55] offset:4096
	s_waitcnt vmcnt(34)
	ds_write_b128 v164, v[56:59] offset:5120
	s_waitcnt vmcnt(33)
	ds_write_b128 v164, v[60:63] offset:6144
	s_waitcnt vmcnt(32)
	ds_write_b128 v164, v[64:67] offset:7168
	s_waitcnt lgkmcnt(0)
	s_barrier
	global_load_dwordx4 v[36:39], v165, s[20:21]
	global_load_dwordx4 v[40:43], v165, s[20:21] offset:1024
	global_load_dwordx4 v[44:47], v165, s[20:21] offset:2048
	global_load_dwordx4 v[48:51], v165, s[20:21] offset:3072
	global_load_dwordx4 v[52:55], v165, s[22:23]
	global_load_dwordx4 v[56:59], v165, s[22:23] offset:1024
	global_load_dwordx4 v[60:63], v165, s[22:23] offset:2048
	global_load_dwordx4 v[64:67], v165, s[22:23] offset:3072
	s_add_u32 s20, s20, 0x1000
	s_addc_u32 s21, s21, 0
	s_add_u32 s22, s22, 0x1000
	s_addc_u32 s23, s23, 0
	s_waitcnt vmcnt(39)
	ds_write_b128 v164, v[68:71] offset:16384
	s_waitcnt vmcnt(38)
	ds_write_b128 v164, v[72:75] offset:17408
	s_waitcnt vmcnt(37)
	ds_write_b128 v164, v[76:79] offset:18432
	s_waitcnt vmcnt(36)
	ds_write_b128 v164, v[80:83] offset:19456
	s_waitcnt vmcnt(35)
	ds_write_b128 v164, v[84:87] offset:20480
	s_waitcnt vmcnt(34)
	ds_write_b128 v164, v[88:91] offset:21504
	s_waitcnt vmcnt(33)
	ds_write_b128 v164, v[92:95] offset:22528
	s_waitcnt vmcnt(32)
	ds_write_b128 v164, v[96:99] offset:23552
	s_waitcnt lgkmcnt(0)
	s_barrier
	global_load_dwordx4 v[68:71], v165, s[20:21]
	global_load_dwordx4 v[72:75], v165, s[20:21] offset:1024
	global_load_dwordx4 v[76:79], v165, s[20:21] offset:2048
	global_load_dwordx4 v[80:83], v165, s[20:21] offset:3072
	global_load_dwordx4 v[84:87], v165, s[22:23]
	global_load_dwordx4 v[88:91], v165, s[22:23] offset:1024
	global_load_dwordx4 v[92:95], v165, s[22:23] offset:2048
	global_load_dwordx4 v[96:99], v165, s[22:23] offset:3072
	s_add_u32 s20, s20, 0x1000
	s_addc_u32 s21, s21, 0
	s_add_u32 s22, s22, 0x1000
	s_addc_u32 s23, s23, 0
	s_waitcnt vmcnt(39)
	ds_write_b128 v164, v[100:103]
	s_waitcnt vmcnt(38)
	ds_write_b128 v164, v[104:107] offset:1024
	s_waitcnt vmcnt(37)
	ds_write_b128 v164, v[108:111] offset:2048
	s_waitcnt vmcnt(36)
	ds_write_b128 v164, v[112:115] offset:3072
	s_waitcnt vmcnt(35)
	ds_write_b128 v164, v[116:119] offset:4096
	s_waitcnt vmcnt(34)
	ds_write_b128 v164, v[120:123] offset:5120
	s_waitcnt vmcnt(33)
	ds_write_b128 v164, v[124:127] offset:6144
	s_waitcnt vmcnt(32)
	ds_write_b128 v164, v[128:131] offset:7168
	s_waitcnt lgkmcnt(0)
	s_barrier
	global_load_dwordx4 v[100:103], v165, s[20:21]
	global_load_dwordx4 v[104:107], v165, s[20:21] offset:1024
	global_load_dwordx4 v[108:111], v165, s[20:21] offset:2048
	global_load_dwordx4 v[112:115], v165, s[20:21] offset:3072
	global_load_dwordx4 v[116:119], v165, s[22:23]
	global_load_dwordx4 v[120:123], v165, s[22:23] offset:1024
	global_load_dwordx4 v[124:127], v165, s[22:23] offset:2048
	global_load_dwordx4 v[128:131], v165, s[22:23] offset:3072
	s_add_u32 s20, s20, 0x1000
	s_addc_u32 s21, s21, 0
	s_add_u32 s22, s22, 0x1000
	s_addc_u32 s23, s23, 0
	s_waitcnt vmcnt(39)
	ds_write_b128 v164, v[132:135] offset:16384
	s_waitcnt vmcnt(38)
	ds_write_b128 v164, v[136:139] offset:17408
	s_waitcnt vmcnt(37)
	ds_write_b128 v164, v[140:143] offset:18432
	s_waitcnt vmcnt(36)
	ds_write_b128 v164, v[144:147] offset:19456
	s_waitcnt vmcnt(35)
	ds_write_b128 v164, v[148:151] offset:20480
	s_waitcnt vmcnt(34)
	ds_write_b128 v164, v[152:155] offset:21504
	s_waitcnt vmcnt(33)
	ds_write_b128 v164, v[156:159] offset:22528
	s_waitcnt vmcnt(32)
	ds_write_b128 v164, v[160:163] offset:23552
	s_waitcnt lgkmcnt(0)
	s_barrier
	global_load_dwordx4 v[132:135], v165, s[20:21]
	global_load_dwordx4 v[136:139], v165, s[20:21] offset:1024
	global_load_dwordx4 v[140:143], v165, s[20:21] offset:2048
	global_load_dwordx4 v[144:147], v165, s[20:21] offset:3072
	global_load_dwordx4 v[148:151], v165, s[22:23]
	global_load_dwordx4 v[152:155], v165, s[22:23] offset:1024
	global_load_dwordx4 v[156:159], v165, s[22:23] offset:2048
	global_load_dwordx4 v[160:163], v165, s[22:23] offset:3072
	s_add_u32 s20, s20, 0x1000
	s_addc_u32 s21, s21, 0
	s_add_u32 s22, s22, 0x1000
	s_addc_u32 s23, s23, 0
	s_waitcnt vmcnt(39)
	ds_write_b128 v164, v[4:7]
	s_waitcnt vmcnt(38)
	ds_write_b128 v164, v[8:11] offset:1024
	s_waitcnt vmcnt(37)
	ds_write_b128 v164, v[12:15] offset:2048
	s_waitcnt vmcnt(36)
	ds_write_b128 v164, v[16:19] offset:3072
	s_waitcnt vmcnt(35)
	ds_write_b128 v164, v[20:23] offset:4096
	s_waitcnt vmcnt(34)
	ds_write_b128 v164, v[24:27] offset:5120
	s_waitcnt vmcnt(33)
	ds_write_b128 v164, v[28:31] offset:6144
	s_waitcnt vmcnt(32)
	ds_write_b128 v164, v[32:35] offset:7168
	s_waitcnt lgkmcnt(0)
	s_barrier
	global_load_dwordx4 v[4:7], v165, s[20:21]
	global_load_dwordx4 v[8:11], v165, s[20:21] offset:1024
	global_load_dwordx4 v[12:15], v165, s[20:21] offset:2048
	global_load_dwordx4 v[16:19], v165, s[20:21] offset:3072
	global_load_dwordx4 v[20:23], v165, s[22:23]
	global_load_dwordx4 v[24:27], v165, s[22:23] offset:1024
	global_load_dwordx4 v[28:31], v165, s[22:23] offset:2048
	global_load_dwordx4 v[32:35], v165, s[22:23] offset:3072
	s_add_u32 s20, s20, 0x1000
	s_addc_u32 s21, s21, 0
	s_add_u32 s22, s22, 0x1000
	s_addc_u32 s23, s23, 0
	s_waitcnt vmcnt(39)
	ds_write_b128 v164, v[36:39] offset:16384
	s_waitcnt vmcnt(38)
	ds_write_b128 v164, v[40:43] offset:17408
	s_waitcnt vmcnt(37)
	ds_write_b128 v164, v[44:47] offset:18432
	s_waitcnt vmcnt(36)
	ds_write_b128 v164, v[48:51] offset:19456
	s_waitcnt vmcnt(35)
	ds_write_b128 v164, v[52:55] offset:20480
	s_waitcnt vmcnt(34)
	ds_write_b128 v164, v[56:59] offset:21504
	s_waitcnt vmcnt(33)
	ds_write_b128 v164, v[60:63] offset:22528
	s_waitcnt vmcnt(32)
	ds_write_b128 v164, v[64:67] offset:23552
	s_waitcnt lgkmcnt(0)
	s_barrier
	s_waitcnt vmcnt(31)
	ds_write_b128 v164, v[68:71]
	s_waitcnt vmcnt(30)
	ds_write_b128 v164, v[72:75] offset:1024
	s_waitcnt vmcnt(29)
	ds_write_b128 v164, v[76:79] offset:2048
	s_waitcnt vmcnt(28)
	ds_write_b128 v164, v[80:83] offset:3072
	s_waitcnt vmcnt(27)
	ds_write_b128 v164, v[84:87] offset:4096
	s_waitcnt vmcnt(26)
	ds_write_b128 v164, v[88:91] offset:5120
	s_waitcnt vmcnt(25)
	ds_write_b128 v164, v[92:95] offset:6144
	s_waitcnt vmcnt(24)
	ds_write_b128 v164, v[96:99] offset:7168
	s_waitcnt lgkmcnt(0)
	s_barrier
	s_waitcnt vmcnt(23)
	ds_write_b128 v164, v[100:103] offset:16384
	s_waitcnt vmcnt(22)
	ds_write_b128 v164, v[104:107] offset:17408
	s_waitcnt vmcnt(21)
	ds_write_b128 v164, v[108:111] offset:18432
	s_waitcnt vmcnt(20)
	ds_write_b128 v164, v[112:115] offset:19456
	s_waitcnt vmcnt(19)
	ds_write_b128 v164, v[116:119] offset:20480
	s_waitcnt vmcnt(18)
	ds_write_b128 v164, v[120:123] offset:21504
	s_waitcnt vmcnt(17)
	ds_write_b128 v164, v[124:127] offset:22528
	s_waitcnt vmcnt(16)
	ds_write_b128 v164, v[128:131] offset:23552
	s_waitcnt lgkmcnt(0)
	s_barrier
	s_waitcnt vmcnt(15)
	ds_write_b128 v164, v[132:135]
	s_waitcnt vmcnt(14)
	ds_write_b128 v164, v[136:139] offset:1024
	s_waitcnt vmcnt(13)
	ds_write_b128 v164, v[140:143] offset:2048
	s_waitcnt vmcnt(12)
	ds_write_b128 v164, v[144:147] offset:3072
	s_waitcnt vmcnt(11)
	ds_write_b128 v164, v[148:151] offset:4096
	s_waitcnt vmcnt(10)
	ds_write_b128 v164, v[152:155] offset:5120
	s_waitcnt vmcnt(9)
	ds_write_b128 v164, v[156:159] offset:6144
	s_waitcnt vmcnt(8)
	ds_write_b128 v164, v[160:163] offset:7168
	s_waitcnt lgkmcnt(0)
	s_barrier
	s_waitcnt vmcnt(7)
	ds_write_b128 v164, v[4:7] offset:16384
	s_waitcnt vmcnt(6)
	ds_write_b128 v164, v[8:11] offset:17408
	s_waitcnt vmcnt(5)
	ds_write_b128 v164, v[12:15] offset:18432
	s_waitcnt vmcnt(4)
	ds_write_b128 v164, v[16:19] offset:19456
	s_waitcnt vmcnt(3)
	ds_write_b128 v164, v[20:23] offset:20480
	s_waitcnt vmcnt(2)
	ds_write_b128 v164, v[24:27] offset:21504
	s_waitcnt vmcnt(1)
	ds_write_b128 v164, v[28:31] offset:22528
	s_waitcnt vmcnt(0)
	ds_write_b128 v164, v[32:35] offset:23552
	s_waitcnt lgkmcnt(0)
	s_barrier
	s_endpgm
	s_nop 0
	s_nop 0
	s_nop 0
	s_nop 0
	s_nop 0
	s_nop 0
	s_nop 0
	s_nop 0
	s_nop 0
	s_nop 0
	s_nop 0
	s_nop 0
	s_nop 0
	s_nop 0
	s_nop 0
	s_nop 0
	s_nop 0
	s_nop 0
	s_nop 0
	s_nop 0
	s_nop 0
	s_nop 0
	s_nop 0
	s_nop 0
	s_nop 0
	s_nop 0
	s_nop 0
	s_nop 0
	s_nop 0
	s_nop 0
	s_nop 0
	s_nop 0
	s_nop 0
	s_nop 0
	s_nop 0
	s_nop 0
	s_nop 0
	s_nop 0
	s_nop 0
	s_nop 0
	s_nop 0
	s_nop 0
	s_nop 0
	s_nop 0
	s_nop 0
	s_nop 0
	s_nop 0
	s_nop 0
	s_nop 0
	s_nop 0
	s_nop 0
	s_nop 0
	s_nop 0
	s_nop 0
	s_nop 0
	s_nop 0
	s_nop 0
	s_nop 0
	s_endpgm

.LBB3_4:
	s_load_dwordx2 s[20:21], s[0:1], 0x0
	s_load_dwordx2 s[24:25], s[0:1], 0x38
	s_mov_b32 s16, s4
	s_mov_b32 s17, s5
	v_mov_b32_e32 v165, v134
	s_lshl_b32 s18, s16, 18
	s_lshl_b32 s19, s17, 17
	s_add_u32 s18, s18, s19
	v_lshl_or_b32 v164, s17, 13, v165
	v_lshlrev_b32_e32 v2, 4, v0
	s_lshl_b32 s28, s16, 14
	s_waitcnt lgkmcnt(0)
	s_add_u32 s20, s20, s18
	s_addc_u32 s21, s21, 0
	s_add_u32 s22, s20, 0x10000
	s_addc_u32 s23, s21, 0
	s_add_u32 s24, s24, s28
	s_addc_u32 s25, s25, 0
	global_load_dwordx4 v[4:7], v165, s[20:21]
	global_load_dwordx4 v[8:11], v165, s[20:21] offset:1024
	global_load_dwordx4 v[12:15], v165, s[20:21] offset:2048
	global_load_dwordx4 v[16:19], v165, s[20:21] offset:3072
	global_load_dwordx4 v[20:23], v165, s[22:23]
	global_load_dwordx4 v[24:27], v165, s[22:23] offset:1024
	global_load_dwordx4 v[28:31], v165, s[22:23] offset:2048
	global_load_dwordx4 v[32:35], v165, s[22:23] offset:3072
	s_add_u32 s20, s20, 0x1000
	s_addc_u32 s21, s21, 0
	s_add_u32 s22, s22, 0x1000
	s_addc_u32 s23, s23, 0
	global_load_dwordx4 v[36:39], v165, s[20:21]
	global_load_dwordx4 v[40:43], v165, s[20:21] offset:1024
	global_load_dwordx4 v[44:47], v165, s[20:21] offset:2048
	global_load_dwordx4 v[48:51], v165, s[20:21] offset:3072
	global_load_dwordx4 v[52:55], v165, s[22:23]
	global_load_dwordx4 v[56:59], v165, s[22:23] offset:1024
	global_load_dwordx4 v[60:63], v165, s[22:23] offset:2048
	global_load_dwordx4 v[64:67], v165, s[22:23] offset:3072
	s_add_u32 s20, s20, 0x1000
	s_addc_u32 s21, s21, 0
	s_add_u32 s22, s22, 0x1000
	s_addc_u32 s23, s23, 0
	global_load_dwordx4 v[68:71], v165, s[20:21]
	global_load_dwordx4 v[72:75], v165, s[20:21] offset:1024
	global_load_dwordx4 v[76:79], v165, s[20:21] offset:2048
	global_load_dwordx4 v[80:83], v165, s[20:21] offset:3072
	global_load_dwordx4 v[84:87], v165, s[22:23]
	global_load_dwordx4 v[88:91], v165, s[22:23] offset:1024
	global_load_dwordx4 v[92:95], v165, s[22:23] offset:2048
	global_load_dwordx4 v[96:99], v165, s[22:23] offset:3072
	s_add_u32 s20, s20, 0x1000
	s_addc_u32 s21, s21, 0
	s_add_u32 s22, s22, 0x1000
	s_addc_u32 s23, s23, 0
	global_load_dwordx4 v[100:103], v165, s[20:21]
	global_load_dwordx4 v[104:107], v165, s[20:21] offset:1024
	global_load_dwordx4 v[108:111], v165, s[20:21] offset:2048
	global_load_dwordx4 v[112:115], v165, s[20:21] offset:3072
	global_load_dwordx4 v[116:119], v165, s[22:23]
	global_load_dwordx4 v[120:123], v165, s[22:23] offset:1024
	global_load_dwordx4 v[124:127], v165, s[22:23] offset:2048
	global_load_dwordx4 v[128:131], v165, s[22:23] offset:3072
	s_add_u32 s20, s20, 0x1000
	s_addc_u32 s21, s21, 0
	s_add_u32 s22, s22, 0x1000
	s_addc_u32 s23, s23, 0
	global_load_dwordx4 v[132:135], v165, s[20:21]
	global_load_dwordx4 v[136:139], v165, s[20:21] offset:1024
	global_load_dwordx4 v[140:143], v165, s[20:21] offset:2048
	global_load_dwordx4 v[144:147], v165, s[20:21] offset:3072
	global_load_dwordx4 v[148:151], v165, s[22:23]
	global_load_dwordx4 v[152:155], v165, s[22:23] offset:1024
	global_load_dwordx4 v[156:159], v165, s[22:23] offset:2048
	global_load_dwordx4 v[160:163], v165, s[22:23] offset:3072
	s_add_u32 s20, s20, 0x1000
	s_addc_u32 s21, s21, 0
	s_add_u32 s22, s22, 0x1000
	s_addc_u32 s23, s23, 0
	s_waitcnt vmcnt(39)
	ds_write_b128 v164, v[4:7]
	s_waitcnt vmcnt(38)
	ds_write_b128 v164, v[8:11] offset:1024
	s_waitcnt vmcnt(37)
	ds_write_b128 v164, v[12:15] offset:2048
	s_waitcnt vmcnt(36)
	ds_write_b128 v164, v[16:19] offset:3072
	s_waitcnt vmcnt(35)
	ds_write_b128 v164, v[20:23] offset:4096
	s_waitcnt vmcnt(34)
	ds_write_b128 v164, v[24:27] offset:5120
	s_waitcnt vmcnt(33)
	ds_write_b128 v164, v[28:31] offset:6144
	s_waitcnt vmcnt(32)
	ds_write_b128 v164, v[32:35] offset:7168
	s_waitcnt lgkmcnt(0)
	s_barrier
	global_load_dwordx4 v[4:7], v165, s[20:21]
	global_load_dwordx4 v[8:11], v165, s[20:21] offset:1024
	global_load_dwordx4 v[12:15], v165, s[20:21] offset:2048
	global_load_dwordx4 v[16:19], v165, s[20:21] offset:3072
	global_load_dwordx4 v[20:23], v165, s[22:23]
	global_load_dwordx4 v[24:27], v165, s[22:23] offset:1024
	global_load_dwordx4 v[28:31], v165, s[22:23] offset:2048
	global_load_dwordx4 v[32:35], v165, s[22:23] offset:3072
	s_add_u32 s20, s20, 0x1000
	s_addc_u32 s21, s21, 0
	s_add_u32 s22, s22, 0x1000
	s_addc_u32 s23, s23, 0
	s_waitcnt vmcnt(39)
	ds_write_b128 v164, v[36:39] offset:16384
	s_waitcnt vmcnt(38)
	ds_write_b128 v164, v[40:43] offset:17408
	s_waitcnt vmcnt(37)
	ds_write_b128 v164, v[44:47] offset:18432
	s_waitcnt vmcnt(36)
	ds_write_b128 v164, v[48:51] offset:19456
	s_waitcnt vmcnt(35)
	ds_write_b128 v164, v[52:55] offset:20480
	s_waitcnt vmcnt(34)
	ds_write_b128 v164, v[56:59] offset:21504
	s_waitcnt vmcnt(33)
	ds_write_b128 v164, v[60:63] offset:22528
	s_waitcnt vmcnt(32)
	ds_write_b128 v164, v[64:67] offset:23552
	s_waitcnt lgkmcnt(0)
	s_barrier
	global_load_dwordx4 v[36:39], v165, s[20:21]
	global_load_dwordx4 v[40:43], v165, s[20:21] offset:1024
	global_load_dwordx4 v[44:47], v165, s[20:21] offset:2048
	global_load_dwordx4 v[48:51], v165, s[20:21] offset:3072
	global_load_dwordx4 v[52:55], v165, s[22:23]
	global_load_dwordx4 v[56:59], v165, s[22:23] offset:1024
	global_load_dwordx4 v[60:63], v165, s[22:23] offset:2048
	global_load_dwordx4 v[64:67], v165, s[22:23] offset:3072
	s_add_u32 s20, s20, 0x1000
	s_addc_u32 s21, s21, 0
	s_add_u32 s22, s22, 0x1000
	s_addc_u32 s23, s23, 0
	s_waitcnt vmcnt(39)
	ds_write_b128 v164, v[68:71]
	s_waitcnt vmcnt(38)
	ds_write_b128 v164, v[72:75] offset:1024
	s_waitcnt vmcnt(37)
	ds_write_b128 v164, v[76:79] offset:2048
	s_waitcnt vmcnt(36)
	ds_write_b128 v164, v[80:83] offset:3072
	s_waitcnt vmcnt(35)
	ds_write_b128 v164, v[84:87] offset:4096
	s_waitcnt vmcnt(34)
	ds_write_b128 v164, v[88:91] offset:5120
	s_waitcnt vmcnt(33)
	ds_write_b128 v164, v[92:95] offset:6144
	s_waitcnt vmcnt(32)
	ds_write_b128 v164, v[96:99] offset:7168
	s_waitcnt lgkmcnt(0)
	s_barrier
	global_load_dwordx4 v[68:71], v165, s[20:21]
	global_load_dwordx4 v[72:75], v165, s[20:21] offset:1024
	global_load_dwordx4 v[76:79], v165, s[20:21] offset:2048
	global_load_dwordx4 v[80:83], v165, s[20:21] offset:3072
	global_load_dwordx4 v[84:87], v165, s[22:23]
	global_load_dwordx4 v[88:91], v165, s[22:23] offset:1024
	global_load_dwordx4 v[92:95], v165, s[22:23] offset:2048
	global_load_dwordx4 v[96:99], v165, s[22:23] offset:3072
	s_add_u32 s20, s20, 0x1000
	s_addc_u32 s21, s21, 0
	s_add_u32 s22, s22, 0x1000
	s_addc_u32 s23, s23, 0
	s_waitcnt vmcnt(39)
	ds_write_b128 v164, v[100:103] offset:16384
	s_waitcnt vmcnt(38)
	ds_write_b128 v164, v[104:107] offset:17408
	s_waitcnt vmcnt(37)
	ds_write_b128 v164, v[108:111] offset:18432
	s_waitcnt vmcnt(36)
	ds_write_b128 v164, v[112:115] offset:19456
	s_waitcnt vmcnt(35)
	ds_write_b128 v164, v[116:119] offset:20480
	s_waitcnt vmcnt(34)
	ds_write_b128 v164, v[120:123] offset:21504
	s_waitcnt vmcnt(33)
	ds_write_b128 v164, v[124:127] offset:22528
	s_waitcnt vmcnt(32)
	ds_write_b128 v164, v[128:131] offset:23552
	s_waitcnt lgkmcnt(0)
	s_barrier
	global_load_dwordx4 v[100:103], v165, s[20:21]
	global_load_dwordx4 v[104:107], v165, s[20:21] offset:1024
	global_load_dwordx4 v[108:111], v165, s[20:21] offset:2048
	global_load_dwordx4 v[112:115], v165, s[20:21] offset:3072
	global_load_dwordx4 v[116:119], v165, s[22:23]
	global_load_dwordx4 v[120:123], v165, s[22:23] offset:1024
	global_load_dwordx4 v[124:127], v165, s[22:23] offset:2048
	global_load_dwordx4 v[128:131], v165, s[22:23] offset:3072
	s_add_u32 s20, s20, 0x1000
	s_addc_u32 s21, s21, 0
	s_add_u32 s22, s22, 0x1000
	s_addc_u32 s23, s23, 0
	s_waitcnt vmcnt(39)
	ds_write_b128 v164, v[132:135]
	s_waitcnt vmcnt(38)
	ds_write_b128 v164, v[136:139] offset:1024
	s_waitcnt vmcnt(37)
	ds_write_b128 v164, v[140:143] offset:2048
	s_waitcnt vmcnt(36)
	ds_write_b128 v164, v[144:147] offset:3072
	s_waitcnt vmcnt(35)
	ds_write_b128 v164, v[148:151] offset:4096
	s_waitcnt vmcnt(34)
	ds_write_b128 v164, v[152:155] offset:5120
	s_waitcnt vmcnt(33)
	ds_write_b128 v164, v[156:159] offset:6144
	s_waitcnt vmcnt(32)
	ds_write_b128 v164, v[160:163] offset:7168
	s_waitcnt lgkmcnt(0)
	s_barrier
	global_load_dwordx4 v[132:135], v165, s[20:21]
	global_load_dwordx4 v[136:139], v165, s[20:21] offset:1024
	global_load_dwordx4 v[140:143], v165, s[20:21] offset:2048
	global_load_dwordx4 v[144:147], v165, s[20:21] offset:3072
	global_load_dwordx4 v[148:151], v165, s[22:23]
	global_load_dwordx4 v[152:155], v165, s[22:23] offset:1024
	global_load_dwordx4 v[156:159], v165, s[22:23] offset:2048
	global_load_dwordx4 v[160:163], v165, s[22:23] offset:3072
	s_add_u32 s20, s20, 0x1000
	s_addc_u32 s21, s21, 0
	s_add_u32 s22, s22, 0x1000
	s_addc_u32 s23, s23, 0
	s_waitcnt vmcnt(39)
	ds_write_b128 v164, v[4:7] offset:16384
	s_waitcnt vmcnt(38)
	ds_write_b128 v164, v[8:11] offset:17408
	s_waitcnt vmcnt(37)
	ds_write_b128 v164, v[12:15] offset:18432
	s_waitcnt vmcnt(36)
	ds_write_b128 v164, v[16:19] offset:19456
	s_waitcnt vmcnt(35)
	ds_write_b128 v164, v[20:23] offset:20480
	s_waitcnt vmcnt(34)
	ds_write_b128 v164, v[24:27] offset:21504
	s_waitcnt vmcnt(33)
	ds_write_b128 v164, v[28:31] offset:22528
	s_waitcnt vmcnt(32)
	ds_write_b128 v164, v[32:35] offset:23552
	s_waitcnt lgkmcnt(0)
	s_barrier
	global_load_dwordx4 v[4:7], v165, s[20:21]
	global_load_dwordx4 v[8:11], v165, s[20:21] offset:1024
	global_load_dwordx4 v[12:15], v165, s[20:21] offset:2048
	global_load_dwordx4 v[16:19], v165, s[20:21] offset:3072
	global_load_dwordx4 v[20:23], v165, s[22:23]
	global_load_dwordx4 v[24:27], v165, s[22:23] offset:1024
	global_load_dwordx4 v[28:31], v165, s[22:23] offset:2048
	global_load_dwordx4 v[32:35], v165, s[22:23] offset:3072
	s_add_u32 s20, s20, 0x1000
	s_addc_u32 s21, s21, 0
	s_add_u32 s22, s22, 0x1000
	s_addc_u32 s23, s23, 0
	s_waitcnt vmcnt(39)
	ds_write_b128 v164, v[36:39]
	s_waitcnt vmcnt(38)
	ds_write_b128 v164, v[40:43] offset:1024
	s_waitcnt vmcnt(37)
	ds_write_b128 v164, v[44:47] offset:2048
	s_waitcnt vmcnt(36)
	ds_write_b128 v164, v[48:51] offset:3072
	s_waitcnt vmcnt(35)
	ds_write_b128 v164, v[52:55] offset:4096
	s_waitcnt vmcnt(34)
	ds_write_b128 v164, v[56:59] offset:5120
	s_waitcnt vmcnt(33)
	ds_write_b128 v164, v[60:63] offset:6144
	s_waitcnt vmcnt(32)
	ds_write_b128 v164, v[64:67] offset:7168
	s_waitcnt lgkmcnt(0)
	s_barrier
	global_load_dwordx4 v[36:39], v165, s[20:21]
	global_load_dwordx4 v[40:43], v165, s[20:21] offset:1024
	global_load_dwordx4 v[44:47], v165, s[20:21] offset:2048
	global_load_dwordx4 v[48:51], v165, s[20:21] offset:3072
	global_load_dwordx4 v[52:55], v165, s[22:23]
	global_load_dwordx4 v[56:59], v165, s[22:23] offset:1024
	global_load_dwordx4 v[60:63], v165, s[22:23] offset:2048
	global_load_dwordx4 v[64:67], v165, s[22:23] offset:3072
	s_add_u32 s20, s20, 0x1000
	s_addc_u32 s21, s21, 0
	s_add_u32 s22, s22, 0x1000
	s_addc_u32 s23, s23, 0
	s_waitcnt vmcnt(39)
	ds_write_b128 v164, v[68:71] offset:16384
	s_waitcnt vmcnt(38)
	ds_write_b128 v164, v[72:75] offset:17408
	s_waitcnt vmcnt(37)
	ds_write_b128 v164, v[76:79] offset:18432
	s_waitcnt vmcnt(36)
	ds_write_b128 v164, v[80:83] offset:19456
	s_waitcnt vmcnt(35)
	ds_write_b128 v164, v[84:87] offset:20480
	s_waitcnt vmcnt(34)
	ds_write_b128 v164, v[88:91] offset:21504
	s_waitcnt vmcnt(33)
	ds_write_b128 v164, v[92:95] offset:22528
	s_waitcnt vmcnt(32)
	ds_write_b128 v164, v[96:99] offset:23552
	s_waitcnt lgkmcnt(0)
	s_barrier
	global_load_dwordx4 v[68:71], v165, s[20:21]
	global_load_dwordx4 v[72:75], v165, s[20:21] offset:1024
	global_load_dwordx4 v[76:79], v165, s[20:21] offset:2048
	global_load_dwordx4 v[80:83], v165, s[20:21] offset:3072
	global_load_dwordx4 v[84:87], v165, s[22:23]
	global_load_dwordx4 v[88:91], v165, s[22:23] offset:1024
	global_load_dwordx4 v[92:95], v165, s[22:23] offset:2048
	global_load_dwordx4 v[96:99], v165, s[22:23] offset:3072
	s_add_u32 s20, s20, 0x1000
	s_addc_u32 s21, s21, 0
	s_add_u32 s22, s22, 0x1000
	s_addc_u32 s23, s23, 0
	s_waitcnt vmcnt(39)
	ds_write_b128 v164, v[100:103]
	s_waitcnt vmcnt(38)
	ds_write_b128 v164, v[104:107] offset:1024
	s_waitcnt vmcnt(37)
	ds_write_b128 v164, v[108:111] offset:2048
	s_waitcnt vmcnt(36)
	ds_write_b128 v164, v[112:115] offset:3072
	s_waitcnt vmcnt(35)
	ds_write_b128 v164, v[116:119] offset:4096
	s_waitcnt vmcnt(34)
	ds_write_b128 v164, v[120:123] offset:5120
	s_waitcnt vmcnt(33)
	ds_write_b128 v164, v[124:127] offset:6144
	s_waitcnt vmcnt(32)
	ds_write_b128 v164, v[128:131] offset:7168
	s_waitcnt lgkmcnt(0)
	s_barrier
	global_load_dwordx4 v[100:103], v165, s[20:21]
	global_load_dwordx4 v[104:107], v165, s[20:21] offset:1024
	global_load_dwordx4 v[108:111], v165, s[20:21] offset:2048
	global_load_dwordx4 v[112:115], v165, s[20:21] offset:3072
	global_load_dwordx4 v[116:119], v165, s[22:23]
	global_load_dwordx4 v[120:123], v165, s[22:23] offset:1024
	global_load_dwordx4 v[124:127], v165, s[22:23] offset:2048
	global_load_dwordx4 v[128:131], v165, s[22:23] offset:3072
	s_add_u32 s20, s20, 0x1000
	s_addc_u32 s21, s21, 0
	s_add_u32 s22, s22, 0x1000
	s_addc_u32 s23, s23, 0
	s_waitcnt vmcnt(39)
	ds_write_b128 v164, v[132:135] offset:16384
	s_waitcnt vmcnt(38)
	ds_write_b128 v164, v[136:139] offset:17408
	s_waitcnt vmcnt(37)
	ds_write_b128 v164, v[140:143] offset:18432
	s_waitcnt vmcnt(36)
	ds_write_b128 v164, v[144:147] offset:19456
	s_waitcnt vmcnt(35)
	ds_write_b128 v164, v[148:151] offset:20480
	s_waitcnt vmcnt(34)
	ds_write_b128 v164, v[152:155] offset:21504
	s_waitcnt vmcnt(33)
	ds_write_b128 v164, v[156:159] offset:22528
	s_waitcnt vmcnt(32)
	ds_write_b128 v164, v[160:163] offset:23552
	s_waitcnt lgkmcnt(0)
	s_barrier
	global_load_dwordx4 v[132:135], v165, s[20:21]
	global_load_dwordx4 v[136:139], v165, s[20:21] offset:1024
	global_load_dwordx4 v[140:143], v165, s[20:21] offset:2048
	global_load_dwordx4 v[144:147], v165, s[20:21] offset:3072
	global_load_dwordx4 v[148:151], v165, s[22:23]
	global_load_dwordx4 v[152:155], v165, s[22:23] offset:1024
	global_load_dwordx4 v[156:159], v165, s[22:23] offset:2048
	global_load_dwordx4 v[160:163], v165, s[22:23] offset:3072
	s_add_u32 s20, s20, 0x1000
	s_addc_u32 s21, s21, 0
	s_add_u32 s22, s22, 0x1000
	s_addc_u32 s23, s23, 0
	s_waitcnt vmcnt(39)
	ds_write_b128 v164, v[4:7]
	s_waitcnt vmcnt(38)
	ds_write_b128 v164, v[8:11] offset:1024
	s_waitcnt vmcnt(37)
	ds_write_b128 v164, v[12:15] offset:2048
	s_waitcnt vmcnt(36)
	ds_write_b128 v164, v[16:19] offset:3072
	s_waitcnt vmcnt(35)
	ds_write_b128 v164, v[20:23] offset:4096
	s_waitcnt vmcnt(34)
	ds_write_b128 v164, v[24:27] offset:5120
	s_waitcnt vmcnt(33)
	ds_write_b128 v164, v[28:31] offset:6144
	s_waitcnt vmcnt(32)
	ds_write_b128 v164, v[32:35] offset:7168
	s_waitcnt lgkmcnt(0)
	s_barrier
	global_load_dwordx4 v[4:7], v165, s[20:21]
	global_load_dwordx4 v[8:11], v165, s[20:21] offset:1024
	global_load_dwordx4 v[12:15], v165, s[20:21] offset:2048
	global_load_dwordx4 v[16:19], v165, s[20:21] offset:3072
	global_load_dwordx4 v[20:23], v165, s[22:23]
	global_load_dwordx4 v[24:27], v165, s[22:23] offset:1024
	global_load_dwordx4 v[28:31], v165, s[22:23] offset:2048
	global_load_dwordx4 v[32:35], v165, s[22:23] offset:3072
	s_add_u32 s20, s20, 0x1000
	s_addc_u32 s21, s21, 0
	s_add_u32 s22, s22, 0x1000
	s_addc_u32 s23, s23, 0
	s_waitcnt vmcnt(39)
	ds_write_b128 v164, v[36:39] offset:16384
	s_waitcnt vmcnt(38)
	ds_write_b128 v164, v[40:43] offset:17408
	s_waitcnt vmcnt(37)
	ds_write_b128 v164, v[44:47] offset:18432
	s_waitcnt vmcnt(36)
	ds_write_b128 v164, v[48:51] offset:19456
	s_waitcnt vmcnt(35)
	ds_write_b128 v164, v[52:55] offset:20480
	s_waitcnt vmcnt(34)
	ds_write_b128 v164, v[56:59] offset:21504
	s_waitcnt vmcnt(33)
	ds_write_b128 v164, v[60:63] offset:22528
	s_waitcnt vmcnt(32)
	ds_write_b128 v164, v[64:67] offset:23552
	s_waitcnt lgkmcnt(0)
	s_barrier
	global_load_dwordx4 v[36:39], v2, s[24:25] offset:-4096
	global_load_dwordx4 v[40:43], v2, s[24:25] offset:-2048
	global_load_dwordx4 v[44:47], v2, s[24:25]
	global_load_dwordx4 v[48:51], v2, s[24:25] offset:2048
	s_add_u32 s24, s24, 0x2000
	s_addc_u32 s25, s25, 0
	global_load_dwordx4 v[52:55], v2, s[24:25] offset:-4096
	global_load_dwordx4 v[56:59], v2, s[24:25] offset:-2048
	global_load_dwordx4 v[60:63], v2, s[24:25]
	global_load_dwordx4 v[64:67], v2, s[24:25] offset:2048
	s_waitcnt vmcnt(39)
	ds_write_b128 v164, v[68:71]
	s_waitcnt vmcnt(38)
	ds_write_b128 v164, v[72:75] offset:1024
	s_waitcnt vmcnt(37)
	ds_write_b128 v164, v[76:79] offset:2048
	s_waitcnt vmcnt(36)
	ds_write_b128 v164, v[80:83] offset:3072
	s_waitcnt vmcnt(35)
	ds_write_b128 v164, v[84:87] offset:4096
	s_waitcnt vmcnt(34)
	ds_write_b128 v164, v[88:91] offset:5120
	s_waitcnt vmcnt(33)
	ds_write_b128 v164, v[92:95] offset:6144
	s_waitcnt vmcnt(32)
	ds_write_b128 v164, v[96:99] offset:7168
	s_waitcnt lgkmcnt(0)
	s_barrier
	s_waitcnt vmcnt(31)
	ds_write_b128 v164, v[100:103] offset:16384
	s_waitcnt vmcnt(30)
	ds_write_b128 v164, v[104:107] offset:17408
	s_waitcnt vmcnt(29)
	ds_write_b128 v164, v[108:111] offset:18432
	s_waitcnt vmcnt(28)
	ds_write_b128 v164, v[112:115] offset:19456
	s_waitcnt vmcnt(27)
	ds_write_b128 v164, v[116:119] offset:20480
	s_waitcnt vmcnt(26)
	ds_write_b128 v164, v[120:123] offset:21504
	s_waitcnt vmcnt(25)
	ds_write_b128 v164, v[124:127] offset:22528
	s_waitcnt vmcnt(24)
	ds_write_b128 v164, v[128:131] offset:23552
	s_waitcnt lgkmcnt(0)
	s_barrier
	s_waitcnt vmcnt(23)
	ds_write_b128 v164, v[132:135]
	s_waitcnt vmcnt(22)
	ds_write_b128 v164, v[136:139] offset:1024
	s_waitcnt vmcnt(21)
	ds_write_b128 v164, v[140:143] offset:2048
	s_waitcnt vmcnt(20)
	ds_write_b128 v164, v[144:147] offset:3072
	s_waitcnt vmcnt(19)
	ds_write_b128 v164, v[148:151] offset:4096
	s_waitcnt vmcnt(18)
	ds_write_b128 v164, v[152:155] offset:5120
	s_waitcnt vmcnt(17)
	ds_write_b128 v164, v[156:159] offset:6144
	s_waitcnt vmcnt(16)
	ds_write_b128 v164, v[160:163] offset:7168
	s_waitcnt lgkmcnt(0)
	s_barrier
	s_waitcnt vmcnt(15)
	ds_write_b128 v164, v[4:7] offset:16384
	s_waitcnt vmcnt(14)
	ds_write_b128 v164, v[8:11] offset:17408
	s_waitcnt vmcnt(13)
	ds_write_b128 v164, v[12:15] offset:18432
	s_waitcnt vmcnt(12)
	ds_write_b128 v164, v[16:19] offset:19456
	s_waitcnt vmcnt(11)
	ds_write_b128 v164, v[20:23] offset:20480
	s_waitcnt vmcnt(10)
	ds_write_b128 v164, v[24:27] offset:21504
	s_waitcnt vmcnt(9)
	ds_write_b128 v164, v[28:31] offset:22528
	s_waitcnt vmcnt(8)
	ds_write_b128 v164, v[32:35] offset:23552
	s_waitcnt lgkmcnt(0)
	s_barrier
	s_waitcnt vmcnt(7)
	ds_write_b128 v2, v[36:39] offset:29696
	s_waitcnt vmcnt(6)
	ds_write_b128 v2, v[40:43] offset:31744
	s_waitcnt vmcnt(5)
	ds_write_b128 v2, v[44:47] offset:33792
	s_waitcnt vmcnt(4)
	ds_write_b128 v2, v[48:51] offset:35840
	s_waitcnt vmcnt(3)
	ds_write_b128 v2, v[52:55] offset:37888
	s_waitcnt vmcnt(2)
	ds_write_b128 v2, v[56:59] offset:39936
	s_waitcnt vmcnt(1)
	ds_write_b128 v2, v[60:63] offset:41984
	s_waitcnt vmcnt(0)
	ds_write_b128 v2, v[64:67] offset:44032
	s_waitcnt lgkmcnt(0)
	s_barrier
	s_endpgm
	s_nop 0
	s_nop 0
	s_nop 0
	s_nop 0
	s_nop 0
	s_endpgm

amdhsa.kernels:
  - .agpr_count:     16
    .args:
      - .actual_access:  read_only
        .address_space:  global
        .offset:         0
        .size:           8
        .value_kind:     global_buffer
      - .actual_access:  read_only
        .address_space:  global
        .offset:         8
        .size:           8
        .value_kind:     global_buffer
      - .actual_access:  read_only
        .address_space:  global
        .offset:         16
        .size:           8
        .value_kind:     global_buffer
      - .actual_access:  read_only
        .address_space:  global
        .offset:         24
        .size:           8
        .value_kind:     global_buffer
      - .actual_access:  write_only
        .address_space:  global
        .offset:         32
        .size:           8
        .value_kind:     global_buffer
      - .actual_access:  write_only
        .address_space:  global
        .offset:         40
        .size:           8
        .value_kind:     global_buffer
      - .actual_access:  write_only
        .address_space:  global
        .offset:         48
        .size:           8
        .value_kind:     global_buffer
      - .actual_access:  write_only
        .address_space:  global
        .offset:         56
        .size:           8
        .value_kind:     global_buffer
      - .actual_access:  read_only
        .address_space:  global
        .offset:         64
        .size:           8
        .value_kind:     global_buffer
      - .actual_access:  read_only
        .address_space:  global
        .offset:         72
        .size:           8
        .value_kind:     global_buffer
      - .actual_access:  read_only
        .address_space:  global
        .offset:         80
        .size:           8
        .value_kind:     global_buffer
    .group_segment_fixed_size: 33792
    .kernarg_segment_align: 8
    .kernarg_segment_size: 88
    .language:       OpenCL C
    .language_version:
      - 2
      - 0
    .max_flat_workgroup_size: 256
    .name:           _Z6k_prepPKfS0_S0_S0_PDF16_S1_S1_S1_S0_S0_S0_
    .private_segment_fixed_size: 0
    .sgpr_count:     22
    .sgpr_spill_count: 0
    .symbol:         _Z6k_prepPKfS0_S0_S0_PDF16_S1_S1_S1_S0_S0_S0_.kd
    .uniform_work_group_size: 1
    .uses_dynamic_stack: false
    .vgpr_count:     184
    .vgpr_spill_count: 0
    .wavefront_size: 64
  - .agpr_count:     0
    .args:
      - .actual_access:  read_only
        .address_space:  global
        .offset:         0
        .size:           8
        .value_kind:     global_buffer
      - .actual_access:  read_only
        .address_space:  global
        .offset:         8
        .size:           8
        .value_kind:     global_buffer
      - .actual_access:  read_only
        .address_space:  global
        .offset:         16
        .size:           8
        .value_kind:     global_buffer
      - .actual_access:  write_only
        .address_space:  global
        .offset:         24
        .size:           8
        .value_kind:     global_buffer
    .group_segment_fixed_size: 0
    .kernarg_segment_align: 8
    .kernarg_segment_size: 32
    .language:       OpenCL C
    .language_version:
      - 2
      - 0
    .max_flat_workgroup_size: 128
    .name:           _Z7k_finalPKfS0_S0_Pf
    .private_segment_fixed_size: 0
    .sgpr_count:     18
    .sgpr_spill_count: 0
    .symbol:         _Z7k_finalPKfS0_S0_Pf.kd
    .uniform_work_group_size: 1
    .uses_dynamic_stack: false
    .vgpr_count:     62
    .vgpr_spill_count: 0
    .wavefront_size: 64
  - .agpr_count:     0
    .args:
      - .actual_access:  read_only
        .address_space:  global
        .offset:         0
        .size:           8
        .value_kind:     global_buffer
      - .actual_access:  read_only
        .address_space:  global
        .offset:         8
        .size:           8
        .value_kind:     global_buffer
      - .actual_access:  read_only
        .address_space:  global
        .offset:         16
        .size:           8
        .value_kind:     global_buffer
      - .actual_access:  read_only
        .address_space:  global
        .offset:         24
        .size:           8
        .value_kind:     global_buffer
      - .actual_access:  read_only
        .address_space:  global
        .offset:         32
        .size:           8
        .value_kind:     global_buffer
      - .actual_access:  write_only
        .address_space:  global
        .offset:         40
        .size:           8
        .value_kind:     global_buffer
      - .actual_access:  write_only
        .address_space:  global
        .offset:         48
        .size:           8
        .value_kind:     global_buffer
      - .actual_access:  read_only
        .address_space:  global
        .offset:         56
        .size:           8
        .value_kind:     global_buffer
      - .actual_access:  read_only
        .address_space:  global
        .offset:         64
        .size:           8
        .value_kind:     global_buffer
    .group_segment_fixed_size: 33808
    .kernarg_segment_align: 8
    .kernarg_segment_size: 72
    .language:       OpenCL C
    .language_version:
      - 2
      - 0
    .max_flat_workgroup_size: 384
    .name:           _Z6k_gemmILi0EEvPKDF16_S1_PKfS3_S1_PDF16_PfS1_S5_
    .private_segment_fixed_size: 0
    .sgpr_count:     20
    .sgpr_spill_count: 0
    .symbol:         _Z6k_gemmILi0EEvPKDF16_S1_PKfS3_S1_PDF16_PfS1_S5_.kd
    .uniform_work_group_size: 1
    .uses_dynamic_stack: false
    .vgpr_count:     166
    .vgpr_spill_count: 0
    .wavefront_size: 64
  - .agpr_count:     0
    .args:
      - .actual_access:  read_only
        .address_space:  global
        .offset:         0
        .size:           8
        .value_kind:     global_buffer
      - .actual_access:  read_only
        .address_space:  global
        .offset:         8
        .size:           8
        .value_kind:     global_buffer
      - .actual_access:  read_only
        .address_space:  global
        .offset:         16
        .size:           8
        .value_kind:     global_buffer
      - .actual_access:  read_only
        .address_space:  global
        .offset:         24
        .size:           8
        .value_kind:     global_buffer
      - .actual_access:  read_only
        .address_space:  global
        .offset:         32
        .size:           8
        .value_kind:     global_buffer
      - .actual_access:  read_only
        .address_space:  global
        .offset:         40
        .size:           8
        .value_kind:     global_buffer
      - .actual_access:  read_only
        .address_space:  global
        .offset:         48
        .size:           8
        .value_kind:     global_buffer
      - .actual_access:  read_only
        .address_space:  global
        .offset:         56
        .size:           8
        .value_kind:     global_buffer
      - .actual_access:  write_only
        .address_space:  global
        .offset:         64
        .size:           8
        .value_kind:     global_buffer
    .group_segment_fixed_size: 50176
    .kernarg_segment_align: 8
    .kernarg_segment_size: 72
    .language:       OpenCL C
    .language_version:
      - 2
      - 0
    .max_flat_workgroup_size: 384
    .name:           _Z6k_gemmILi1EEvPKDF16_S1_PKfS3_S1_PDF16_PfS1_S5_
    .private_segment_fixed_size: 0
    .sgpr_count:     20
    .sgpr_spill_count: 0
    .symbol:         _Z6k_gemmILi1EEvPKDF16_S1_PKfS3_S1_PDF16_PfS1_S5_.kd
    .uniform_work_group_size: 1
    .uses_dynamic_stack: false
    .vgpr_count:     182
    .vgpr_spill_count: 0
    .wavefront_size: 64
